# speedup vs baseline: 1.0335x; 1.0031x over previous
_Z15gemm_out_kernelPKDF16_S0_Pf:
	s_load_dwordx4 s[16:19], s[0:1], 0x0
	s_load_dwordx2 s[4:5], s[0:1], 0x10
	s_lshl_b32 s0, s2, 2
	s_and_b32 s0, s0, 28
	s_bfe_u32 s1, s2, 0x20003
	s_lshr_b32 s8, s2, 5
	v_readfirstlane_b32 s10, v0
	s_or_b32 s9, s0, s1
	s_lshr_b32 s13, s10, 6
	s_mov_b32 s1, 0
	s_lshl_b32 s0, s8, 1
	s_lshr_b32 s14, s10, 8
	s_lshl_b32 s2, s9, 19
	s_lshl_b64 s[6:7], s[0:1], 19
	s_lshl_b32 s0, s13, 10
	s_waitcnt lgkmcnt(0)
	s_add_u32 s2, s16, s2
	s_addc_u32 s3, s17, 0
	s_add_i32 s0, s0, 0
	v_lshlrev_b32_e32 v64, 4, v0
	s_mov_b32 m0, s0
	v_or_b32_e32 v66, 0x2000, v64
	global_load_lds_dwordx4 v64, s[2:3]
	s_add_i32 m0, s0, 0x2000
	v_mov_b32_e32 v67, 0
	s_add_u32 s6, s18, s6
	v_mov_b32_e32 v65, v67
	global_load_lds_dwordx4 v66, s[2:3]
	s_addc_u32 s7, s19, s7
	s_add_i32 m0, s0, 0x4000
	v_lshl_add_u64 v[68:69], s[6:7], 0, v[64:65]
	global_load_lds_dwordx4 v64, s[6:7]
	s_mov_b64 s[20:21], s[6:7]
	s_mov_b64 s[6:7], 0x2000
	v_lshl_add_u64 v[2:3], v[68:69], 0, s[6:7]
	s_add_i32 m0, s0, 0x6000
	s_mov_b64 s[16:17], 0x80000
	global_load_lds_dwordx4 v[2:3], off
	s_add_i32 m0, s0, 0x8000
	v_lshl_add_u64 v[70:71], v[68:69], 0, s[16:17]
	global_load_lds_dwordx4 v[70:71], off
	s_mov_b64 s[16:17], 0x82000
	s_add_i32 m0, s0, 0xa000
	v_lshl_add_u64 v[72:73], v[68:69], 0, s[16:17]
	s_add_u32 s18, s2, 0x4000
	global_load_lds_dwordx4 v[72:73], off
	s_addc_u32 s19, s3, 0
	s_add_i32 m0, s0, 0xc000
	s_mov_b64 s[16:17], 0x4000
	global_load_lds_dwordx4 v64, s[18:19]
	s_add_i32 m0, s0, 0xe000
	v_lshl_add_u64 v[2:3], v[68:69], 0, s[16:17]
	global_load_lds_dwordx4 v66, s[18:19]
	s_add_i32 m0, s0, 0x10000
	s_mov_b64 s[16:17], 0x6000
	global_load_lds_dwordx4 v[2:3], off
	v_lshl_add_u64 v[2:3], v[68:69], 0, s[16:17]
	s_add_i32 m0, s0, 0x12000
	s_mov_b64 s[16:17], 0x84000
	global_load_lds_dwordx4 v[2:3], off
	s_add_i32 m0, s0, 0x14000
	v_lshl_add_u64 v[2:3], v[68:69], 0, s[16:17]
	s_mov_b64 s[16:17], 0x86000
	global_load_lds_dwordx4 v[2:3], off
	v_lshl_add_u64 v[2:3], v[68:69], 0, s[16:17]
	s_add_i32 m0, s0, 0x16000
	s_mov_b32 s12, 2
	global_load_lds_dwordx4 v[2:3], off
	s_waitcnt vmcnt(6)
	s_cmp_lg_u32 s14, 1
	s_barrier
	s_cbranch_scc1 .LBB2_2
	s_barrier

.LBB2_3:
	s_cmp_lt_u32 s14, 30
	s_cselect_b32 s16, 2, 0xffffffe2
	s_add_i32 s16, s16, s14
	s_ashr_i32 s17, s16, 31
	s_mul_i32 s15, s1, 0xc000
	s_lshl_b64 s[16:17], s[16:17], 14
	v_add_u32_e32 v106, s15, v77
	v_add_u32_e32 v138, s15, v76
	s_mul_i32 s15, s12, 0xc000
	s_add_u32 s18, s2, s16
	s_addc_u32 s19, s3, s17
	s_add_i32 s15, s0, s15
	s_add_u32 s22, s20, s16
	s_addc_u32 s23, s21, s17
	s_add_u32 s24, s22, 0x80000
	s_addc_u32 s25, s23, 0
	s_mov_b32 m0, s15
	ds_read_b128 v[78:81], v106 offset:16384
	ds_read_b128 v[82:85], v106 offset:17408
	ds_read_b128 v[86:89], v106 offset:32768
	ds_read_b128 v[90:93], v106 offset:33792
	ds_read_b128 v[94:97], v106 offset:18432
	ds_read_b128 v[98:101], v106 offset:19456
	ds_read_b128 v[102:105], v106 offset:34816
	ds_read_b128 v[106:109], v106 offset:35840
	ds_read_b128 v[110:113], v138
	ds_read_b128 v[114:117], v138 offset:1024
	ds_read_b128 v[118:121], v138 offset:2048
	ds_read_b128 v[122:125], v138 offset:3072
	ds_read_b128 v[126:129], v138 offset:4096
	ds_read_b128 v[130:133], v138 offset:5120
	ds_read_b128 v[134:137], v138 offset:6144
	ds_read_b128 v[138:141], v138 offset:7168
	global_load_lds_dwordx4 v64, s[18:19]
	s_add_i32 m0, s15, 0x2000
	s_nop 0
	global_load_lds_dwordx4 v66, s[18:19]
	s_add_i32 m0, s15, 0x4000
	s_nop 0
	global_load_lds_dwordx4 v64, s[22:23]
	s_waitcnt vmcnt(3) lgkmcnt(0)
	s_barrier
	s_setprio 1
	v_mfma_f32_16x16x32_f16 v[8:11], v[78:81], v[110:113], v[8:11]
	s_add_i32 s18, s15, 0xa000
	v_mfma_f32_16x16x32_f16 v[24:27], v[94:97], v[110:113], v[24:27]
	s_add_i32 s16, s15, 0x8000
	s_add_i32 m0, s15, 0x6000
	v_mfma_f32_16x16x32_f16 v[8:11], v[82:85], v[114:117], v[8:11]
	v_mfma_f32_16x16x32_f16 v[24:27], v[98:101], v[114:117], v[24:27]
	global_load_lds_dwordx4 v66, s[22:23]
	v_mfma_f32_16x16x32_f16 v[12:15], v[78:81], v[118:121], v[12:15]
	v_mfma_f32_16x16x32_f16 v[28:31], v[94:97], v[118:121], v[28:31]
	v_mfma_f32_16x16x32_f16 v[12:15], v[82:85], v[122:125], v[12:15]
	v_mfma_f32_16x16x32_f16 v[28:31], v[98:101], v[122:125], v[28:31]
	v_mfma_f32_16x16x32_f16 v[0:3], v[78:81], v[126:129], v[0:3]
	v_mfma_f32_16x16x32_f16 v[16:19], v[94:97], v[126:129], v[16:19]
	v_mfma_f32_16x16x32_f16 v[0:3], v[82:85], v[130:133], v[0:3]
	v_mfma_f32_16x16x32_f16 v[16:19], v[98:101], v[130:133], v[16:19]
	s_mov_b32 m0, s16
	v_mfma_f32_16x16x32_f16 v[4:7], v[78:81], v[134:137], v[4:7]
	global_load_lds_dwordx4 v64, s[24:25]
	v_mfma_f32_16x16x32_f16 v[20:23], v[94:97], v[134:137], v[20:23]
	v_mfma_f32_16x16x32_f16 v[4:7], v[82:85], v[138:141], v[4:7]
	v_mfma_f32_16x16x32_f16 v[20:23], v[98:101], v[138:141], v[20:23]
	v_mfma_f32_16x16x32_f16 v[40:43], v[86:89], v[110:113], v[40:43]
	v_mfma_f32_16x16x32_f16 v[56:59], v[102:105], v[110:113], v[56:59]
	v_mfma_f32_16x16x32_f16 v[40:43], v[90:93], v[114:117], v[40:43]
	v_mfma_f32_16x16x32_f16 v[56:59], v[106:109], v[114:117], v[56:59]
	s_mov_b32 m0, s18
	v_mfma_f32_16x16x32_f16 v[48:51], v[86:89], v[118:121], v[48:51]
	global_load_lds_dwordx4 v66, s[24:25]
	v_mfma_f32_16x16x32_f16 v[60:63], v[102:105], v[118:121], v[60:63]
	v_mfma_f32_16x16x32_f16 v[48:51], v[90:93], v[122:125], v[48:51]
	v_mfma_f32_16x16x32_f16 v[60:63], v[106:109], v[122:125], v[60:63]
	v_mfma_f32_16x16x32_f16 v[36:39], v[86:89], v[126:129], v[36:39]
	v_mfma_f32_16x16x32_f16 v[52:55], v[102:105], v[126:129], v[52:55]
	v_mfma_f32_16x16x32_f16 v[36:39], v[90:93], v[130:133], v[36:39]
	v_mfma_f32_16x16x32_f16 v[52:55], v[106:109], v[130:133], v[52:55]
	v_mfma_f32_16x16x32_f16 v[32:35], v[86:89], v[134:137], v[32:35]
	v_mfma_f32_16x16x32_f16 v[44:47], v[102:105], v[134:137], v[44:47]
	v_mfma_f32_16x16x32_f16 v[32:35], v[90:93], v[138:141], v[32:35]
	v_mfma_f32_16x16x32_f16 v[44:47], v[106:109], v[138:141], v[44:47]
	s_setprio 0
	s_barrier
	s_add_i32 s15, s1, 1
	s_cmp_lg_u32 s1, 2
	s_cselect_b32 s1, s15, 0
	s_add_i32 s15, s12, 1
	s_cmp_lg_u32 s12, 2
	s_cselect_b32 s12, s15, 0
	s_add_i32 s14, s14, 1
	s_cmp_eq_u32 s14, 32
	s_cbranch_scc0 .LBB2_3
	s_cmpk_lt_u32 s10, 0x100
	s_cbranch_scc0 .LBB2_6
	s_barrier

	.amdhsa_kernel _Z15gemm_out_kernelPKDF16_S0_Pf
		.amdhsa_group_segment_fixed_size 0
		.amdhsa_private_segment_fixed_size 0
		.amdhsa_kernarg_size 24
		.amdhsa_user_sgpr_count 2
		.amdhsa_user_sgpr_dispatch_ptr 0
		.amdhsa_user_sgpr_queue_ptr 0
		.amdhsa_user_sgpr_kernarg_segment_ptr 1
		.amdhsa_user_sgpr_dispatch_id 0
		.amdhsa_user_sgpr_kernarg_preload_length 0
		.amdhsa_user_sgpr_kernarg_preload_offset 0
		.amdhsa_user_sgpr_private_segment_size 0
		.amdhsa_uses_dynamic_stack 0
		.amdhsa_enable_private_segment 0
		.amdhsa_system_sgpr_workgroup_id_x 1
		.amdhsa_system_sgpr_workgroup_id_y 0
		.amdhsa_system_sgpr_workgroup_id_z 0
		.amdhsa_system_sgpr_workgroup_info 0
		.amdhsa_system_vgpr_workitem_id 0
		.amdhsa_next_free_vgpr 148
		.amdhsa_next_free_sgpr 26
		.amdhsa_accum_offset 148
		.amdhsa_reserve_vcc 0
		.amdhsa_float_round_mode_32 0
		.amdhsa_float_round_mode_16_64 0
		.amdhsa_float_denorm_mode_32 3
		.amdhsa_float_denorm_mode_16_64 3
		.amdhsa_dx10_clamp 1
		.amdhsa_ieee_mode 1
		.amdhsa_fp16_overflow 0
		.amdhsa_tg_split 0
		.amdhsa_exception_fp_ieee_invalid_op 0
		.amdhsa_exception_fp_denorm_src 0
		.amdhsa_exception_fp_ieee_div_zero 0
		.amdhsa_exception_fp_ieee_overflow 0
		.amdhsa_exception_fp_ieee_underflow 0
		.amdhsa_exception_fp_ieee_inexact 0
		.amdhsa_exception_int_div_zero 0
	.end_amdhsa_kernel

amdhsa.kernels:
  - .agpr_count:     0
    .args:
      - .actual_access:  read_only
        .address_space:  global
        .offset:         0
        .size:           8
        .value_kind:     global_buffer
      - .actual_access:  read_only
        .address_space:  global
        .offset:         8
        .size:           8
        .value_kind:     global_buffer
      - .actual_access:  read_only
        .address_space:  global
        .offset:         16
        .size:           8
        .value_kind:     global_buffer
      - .actual_access:  write_only
        .address_space:  global
        .offset:         24
        .size:           8
        .value_kind:     global_buffer
      - .actual_access:  write_only
        .address_space:  global
        .offset:         32
        .size:           8
        .value_kind:     global_buffer
      - .actual_access:  write_only
        .address_space:  global
        .offset:         40
        .size:           8
        .value_kind:     global_buffer
      - .actual_access:  write_only
        .address_space:  global
        .offset:         48
        .size:           8
        .value_kind:     global_buffer
    .group_segment_fixed_size: 0
    .kernarg_segment_align: 8
    .kernarg_segment_size: 56
    .language:       OpenCL C
    .language_version:
      - 2
      - 0
    .max_flat_workgroup_size: 1024
    .name:           _Z11prep_kernelPKfS0_PKiPDF16_S3_PfS4_
    .private_segment_fixed_size: 0
    .sgpr_count:     24
    .sgpr_spill_count: 0
    .symbol:         _Z11prep_kernelPKfS0_PKiPDF16_S3_PfS4_.kd
    .uniform_work_group_size: 1
    .uses_dynamic_stack: false
    .vgpr_count:     40
    .vgpr_spill_count: 0
    .wavefront_size: 64
  - .agpr_count:     0
    .args:
      - .address_space:  global
        .offset:         0
        .size:           8
        .value_kind:     global_buffer
      - .address_space:  global
        .offset:         8
        .size:           8
        .value_kind:     global_buffer
      - .address_space:  global
        .offset:         16
        .size:           8
        .value_kind:     global_buffer
      - .address_space:  global
        .offset:         24
        .size:           8
        .value_kind:     global_buffer
      - .address_space:  global
        .offset:         32
        .size:           8
        .value_kind:     global_buffer
      - .address_space:  global
        .offset:         40
        .size:           8
        .value_kind:     global_buffer
      - .address_space:  global
        .offset:         48
        .size:           8
        .value_kind:     global_buffer
      - .address_space:  global
        .offset:         56
        .size:           8
        .value_kind:     global_buffer
      - .address_space:  global
        .offset:         64
        .size:           8
        .value_kind:     global_buffer
      - .address_space:  global
        .offset:         72
        .size:           8
        .value_kind:     global_buffer
      - .address_space:  global
        .offset:         80
        .size:           8
        .value_kind:     global_buffer
      - .address_space:  global
        .offset:         88
        .size:           8
        .value_kind:     global_buffer
      - .address_space:  global
        .offset:         96
        .size:           8
        .value_kind:     global_buffer
      - .address_space:  global
        .offset:         104
        .size:           8
        .value_kind:     global_buffer
    .group_segment_fixed_size: 0
    .kernarg_segment_align: 8
    .kernarg_segment_size: 112
    .language:       OpenCL C
    .language_version:
      - 2
      - 0
    .max_flat_workgroup_size: 512
    .name:           _Z15gemm_qkv_kernelPKDF16_S0_PDF16_S1_S1_PKfS3_S3_S3_S3_S1_PKiPyPj
    .private_segment_fixed_size: 0
    .sgpr_count:     100
    .sgpr_spill_count: 0
    .symbol:         _Z15gemm_qkv_kernelPKDF16_S0_PDF16_S1_S1_PKfS3_S3_S3_S3_S1_PKiPyPj.kd
    .uniform_work_group_size: 1
    .uses_dynamic_stack: false
    .vgpr_count:     248
    .vgpr_spill_count: 0
    .wavefront_size: 64
  - .agpr_count:     0
    .args:
      - .address_space:  global
        .offset:         0
        .size:           8
        .value_kind:     global_buffer
      - .address_space:  global
        .offset:         8
        .size:           8
        .value_kind:     global_buffer
      - .address_space:  global
        .offset:         16
        .size:           8
        .value_kind:     global_buffer
    .group_segment_fixed_size: 0
    .kernarg_segment_align: 8
    .kernarg_segment_size: 24
    .language:       OpenCL C
    .language_version:
      - 2
      - 0
    .max_flat_workgroup_size: 512
    .name:           _Z15gemm_out_kernelPKDF16_S0_Pf
    .private_segment_fixed_size: 0
    .sgpr_count:     32
    .sgpr_spill_count: 0
    .symbol:         _Z15gemm_out_kernelPKDF16_S0_Pf.kd
    .uniform_work_group_size: 1
    .uses_dynamic_stack: false
    .vgpr_count:     148
    .vgpr_spill_count: 0
    .wavefront_size: 64
  - .agpr_count:     0
    .args:
      - .address_space:  global
        .offset:         0
        .size:           8
        .value_kind:     global_buffer
      - .address_space:  global
        .offset:         8
        .size:           8
        .value_kind:     global_buffer
      - .address_space:  global
        .offset:         16
        .size:           8
        .value_kind:     global_buffer
      - .address_space:  global
        .offset:         24
        .size:           8
        .value_kind:     global_buffer
      - .address_space:  global
        .offset:         32
        .size:           8
        .value_kind:     global_buffer
      - .address_space:  global
        .offset:         40
        .size:           8
        .value_kind:     global_buffer
    .group_segment_fixed_size: 0
    .kernarg_segment_align: 8
    .kernarg_segment_size: 48
    .language:       OpenCL C
    .language_version:
      - 2
      - 0
    .max_flat_workgroup_size: 512
    .name:           _Z11attn_kernelPKDF16_S0_S0_PDF16_PKjS3_
    .private_segment_fixed_size: 0
    .sgpr_count:     68
    .sgpr_spill_count: 0
    .symbol:         _Z11attn_kernelPKDF16_S0_S0_PDF16_PKjS3_.kd
    .uniform_work_group_size: 1
    .uses_dynamic_stack: false
    .vgpr_count:     248
    .vgpr_spill_count: 0
    .wavefront_size: 64
